# v38 + lru_local conv-input row loads hoisted to unit start (prologue de-serialization: 7 dependent round trips -> 0)
# speedup vs baseline: 1.0127x; 1.0064x over previous
; DI float bflo(unsigned w) { return __uint_as_float(w << 16); }
; DI float bfhi(unsigned w) { return __uint_as_float(w & 0xffff0000u); }
; DI u32x2 pack4(f32x4 v) { bf16x4_t r = __builtin_convertvector(v, bf16x4_t); return __builtin_bit_cast(u32x2, r); }
; DI int lane_id() { int l; asm volatile("v_mbcnt_lo_u32_b32 %0, -1, 0\n\tv_mbcnt_hi_u32_b32 %0, -1, %0" : "=v"(l)); return l; }
; DI KPtr kargs() { KPtr p = (KPtr)__builtin_amdgcn_kernarg_segment_ptr(); asm volatile("" : "+s"(p)); return p; }
; DI void lru_local_unit(const Ctx& c, int u) {
;     const KPtr kp = kargs();
;     const int blk = u & 7, n = (u >> 3) & 15, b = u >> 7;
;     const int t0 = b * SEQ + n * CHUNK, cb = blk * 128;
;     const unsigned base = (unsigned)(size_t)c.lds, Aimg = base, Waimg = base + IMG_R, Wximg = base + IMG_R + IMG_T;
;     const u16* proj = (const u16*)(c.ws + WS_PROJ);
;     const float* conv_w = kp->in[4]; const float* conv_b = kp->in[5];
;     __syncthreads();
;     {
;         const float* wa = kp->in[6] + (size_t)blk * 16384; const float* wx = kp->in[8] + (size_t)blk * 16384;
;         const int tid = c.wid * 64 + lane_id();
; #pragma unroll
;         for (int it = 0; it < 8; ++it) { const int item = tid + it * NTHR, i = item >> 5, jc = item & 31;
;             *LP(u32x2, Waimg + trrow(i) * TS + jc * 8) = pack4(*(const f32x4*)(wa + i * 128 + jc * 4));
;             *LP(u32x2, Wximg + trrow(i) * TS + jc * 8) = pack4(*(const f32x4*)(wx + i * 128 + jc * 4)); }
;     ...
;         for (int rr = 0; rr < 7; ++rr) { const int tl = 4 * tr - 3 + rr;
;             if (n == 0 && tl < 0) {
; #pragma unroll
;                 for (int k = 0; k < 8; ++k) xin[rr][k] = 0.f;
;             } else { const u32x4 v = *(const u32x4*)(proj + (size_t)(t0 + tl) * INC + 4 * RW + ch);
;                 xin[rr][0] = bflo(v.x); xin[rr][1] = bfhi(v.x); xin[rr][2] = bflo(v.y); xin[rr][3] = bfhi(v.y); xin[rr][4] = bflo(v.z); xin[rr][5] = bfhi(v.z); xin[rr][6] = bflo(v.w); xin[rr][7] = bfhi(v.w); } }
.LBB0_133:
	s_mov_b64 s[24:25], s[0:1]
	s_bfe_u32 s67, s65, 0x40003
	s_ashr_i32 s68, s65, 7
	s_lshl_b32 s8, s68, 11
	s_lshl_b32 s9, s67, 7
	s_or_b32 s66, s9, s8
	s_load_dwordx4 s[8:11], s[24:25], 0x20
	s_load_dwordx2 s[28:29], s[24:25], 0x30
	s_load_dwordx2 s[30:31], s[24:25], 0x40
	s_and_b32 s26, s65, 7
	s_waitcnt lgkmcnt(0)
	s_barrier
	v_mbcnt_lo_u32_b32 v0, -1, 0
	v_mbcnt_hi_u32_b32 v0, -1, v0
	s_lshl_b32 s98, s26, 7
	s_add_u32 s100, s34, 0x2512000
	s_addc_u32 s101, s35, 0
	v_add_u32_e32 v215, s58, v0
	v_and_b32_e32 v212, 15, v0
	v_ashrrev_i32_e32 v215, 2, v215
	v_lshl_or_b32 v212, v212, 3, s98
	v_and_b32_e32 v216, -4, v215
	v_lshlrev_b32_e32 v212, 1, v212
	v_mov_b32_e32 v213, 0
	v_lshl_add_u64 v[210:211], s[100:101], 0, v[212:213]
	v_add3_u32 v214, s66, -3, v216
	v_mad_i64_i32 v[196:197], vcc, v214, s51, v[210:211]
	global_load_dwordx4 v[168:171], v[196:197], off
	v_add3_u32 v214, s66, -2, v216
	v_mad_i64_i32 v[198:199], vcc, v214, s51, v[210:211]
	global_load_dwordx4 v[172:175], v[198:199], off
	v_add3_u32 v214, s66, -1, v216
	v_mad_i64_i32 v[200:201], vcc, v214, s51, v[210:211]
	global_load_dwordx4 v[176:179], v[200:201], off
	v_add_u32_e32 v214, s66, v216
	v_mad_i64_i32 v[202:203], vcc, v214, s51, v[210:211]
	global_load_dwordx4 v[180:183], v[202:203], off
	v_add3_u32 v214, s66, v216, 1
	v_mad_i64_i32 v[204:205], vcc, v214, s51, v[210:211]
	global_load_dwordx4 v[184:187], v[204:205], off
	v_add3_u32 v214, s66, v216, 2
	v_mad_i64_i32 v[206:207], vcc, v214, s51, v[210:211]
	global_load_dwordx4 v[188:191], v[206:207], off
	v_add3_u32 v214, s66, v216, 3
	v_mad_i64_i32 v[208:209], vcc, v214, s51, v[210:211]
	global_load_dwordx4 v[192:195], v[208:209], off
	s_lshl_b32 s27, s26, 16
	v_add_u32_e32 v58, s58, v0
	v_ashrrev_i32_e32 v66, 5, v58
	s_add_u32 s28, s28, s27
	v_and_b32_e32 v46, 31, v0
	v_lshlrev_b32_e32 v0, 7, v66
	s_addc_u32 s29, s29, 0
	v_lshlrev_b32_e32 v88, 4, v46
	v_ashrrev_i32_e32 v1, 31, v0
	v_lshl_add_u64 v[56:57], s[28:29], 0, v[88:89]
	v_lshlrev_b64 v[4:5], 2, v[0:1]
	v_lshl_add_u64 v[0:1], v[56:57], 0, v[4:5]
	global_load_dwordx4 v[0:3], v[0:1], off
	s_add_u32 s28, s30, s27
	s_addc_u32 s29, s31, 0
	v_lshl_add_u64 v[60:61], s[28:29], 0, v[88:89]
	v_add_u32_e32 v8, 0x200, v58
	v_lshl_add_u64 v[4:5], v[60:61], 0, v[4:5]
	v_ashrrev_i32_e32 v67, 5, v8
	global_load_dwordx4 v[4:7], v[4:5], off
	v_lshlrev_b32_e32 v8, 7, v67
	v_ashrrev_i32_e32 v9, 31, v8
	v_lshlrev_b64 v[12:13], 2, v[8:9]
	v_lshl_add_u64 v[8:9], v[56:57], 0, v[12:13]
	v_add_u32_e32 v16, 0x400, v58
	global_load_dwordx4 v[8:11], v[8:9], off
	v_lshl_add_u64 v[12:13], v[60:61], 0, v[12:13]
	v_ashrrev_i32_e32 v68, 5, v16
	global_load_dwordx4 v[12:15], v[12:13], off
	v_lshlrev_b32_e32 v16, 7, v68
	v_ashrrev_i32_e32 v17, 31, v16
	v_lshlrev_b64 v[20:21], 2, v[16:17]
	v_lshl_add_u64 v[16:17], v[56:57], 0, v[20:21]
	v_add_u32_e32 v24, 0x600, v58
	global_load_dwordx4 v[16:19], v[16:17], off
	v_lshl_add_u64 v[20:21], v[60:61], 0, v[20:21]
	v_ashrrev_i32_e32 v69, 5, v24
	global_load_dwordx4 v[20:23], v[20:21], off
	v_lshlrev_b32_e32 v24, 7, v69
	v_ashrrev_i32_e32 v25, 31, v24
	v_lshlrev_b64 v[28:29], 2, v[24:25]
	v_lshl_add_u64 v[24:25], v[56:57], 0, v[28:29]
	v_add_u32_e32 v32, 0x800, v58
	global_load_dwordx4 v[24:27], v[24:25], off
	v_lshl_add_u64 v[28:29], v[60:61], 0, v[28:29]
	v_ashrrev_i32_e32 v70, 5, v32
	global_load_dwordx4 v[28:31], v[28:29], off
	v_lshlrev_b32_e32 v32, 7, v70
	v_ashrrev_i32_e32 v33, 31, v32
	v_lshlrev_b64 v[36:37], 2, v[32:33]
	v_lshl_add_u64 v[32:33], v[56:57], 0, v[36:37]
	v_add_u32_e32 v40, 0xa00, v58
	global_load_dwordx4 v[32:35], v[32:33], off
	v_lshl_add_u64 v[36:37], v[60:61], 0, v[36:37]
	v_ashrrev_i32_e32 v71, 5, v40
	global_load_dwordx4 v[36:39], v[36:37], off
	v_lshlrev_b32_e32 v40, 7, v71
	v_ashrrev_i32_e32 v41, 31, v40
	v_lshlrev_b64 v[44:45], 2, v[40:41]
	v_lshl_add_u64 v[40:41], v[56:57], 0, v[44:45]
	v_add_u32_e32 v48, 0xc00, v58
	global_load_dwordx4 v[40:43], v[40:41], off
	v_lshl_add_u64 v[44:45], v[60:61], 0, v[44:45]
	v_ashrrev_i32_e32 v72, 5, v48
	v_lshlrev_b32_e32 v54, 3, v46
	global_load_dwordx4 v[44:47], v[44:45], off
	v_lshlrev_b32_e32 v48, 7, v72
	v_ashrrev_i32_e32 v49, 31, v48
	v_lshlrev_b64 v[52:53], 2, v[48:49]
	v_lshl_add_u64 v[48:49], v[56:57], 0, v[52:53]
	v_add_u32_e32 v58, 0xe00, v58
	global_load_dwordx4 v[48:51], v[48:49], off
	v_lshl_add_u64 v[52:53], v[60:61], 0, v[52:53]
	v_ashrrev_i32_e32 v75, 5, v58
	v_add_u32_e32 v73, s48, v54
	v_add_u32_e32 v74, s49, v54
	global_load_dwordx4 v[52:55], v[52:53], off
	v_lshlrev_b32_e32 v58, 7, v75
	v_ashrrev_i32_e32 v59, 31, v58
	v_lshlrev_b64 v[62:63], 2, v[58:59]
	v_lshl_add_u64 v[56:57], v[56:57], 0, v[62:63]
	global_load_dwordx4 v[56:59], v[56:57], off
	s_lshl_b32 s70, s26, 7
	s_cmp_eq_u32 s67, 0
	s_cselect_b64 s[26:27], -1, 0
	s_cmp_lg_u32 s67, 0
	s_cselect_b64 s[28:29], -1, 0
	s_waitcnt vmcnt(14)
	v_cvt_pk_bf16_f32 v64, v0, v1
	v_lshrrev_b32_e32 v0, 1, v66
	v_bitop3_b32 v0, v0, v66, 4 bitop3:0x6c
	v_mul_lo_u32 v66, v0, s50
	v_lshl_add_u64 v[0:1], v[60:61], 0, v[62:63]
	v_cvt_pk_bf16_f32 v65, v2, v3
	global_load_dwordx4 v[0:3], v[0:1], off
	v_add_u32_e32 v60, v66, v73
	s_waitcnt vmcnt(14)
	v_cvt_pk_bf16_f32 v7, v6, v7
	v_cvt_pk_bf16_f32 v6, v4, v5
	v_add_u32_e32 v4, v66, v74
	ds_write_b64 v60, v[64:65]
	ds_write_b64 v4, v[6:7]
	v_lshrrev_b32_e32 v6, 1, v67
	v_bitop3_b32 v6, v6, v67, 4 bitop3:0x6c
	v_mul_lo_u32 v6, v6, s50
	s_waitcnt vmcnt(13)
	v_cvt_pk_bf16_f32 v5, v10, v11
	v_cvt_pk_bf16_f32 v4, v8, v9
	v_add_u32_e32 v7, v6, v73
	ds_write_b64 v7, v[4:5]
	s_waitcnt vmcnt(12)
; DI float bflo(unsigned w) { return __uint_as_float(w << 16); }
; DI float bfhi(unsigned w) { return __uint_as_float(w & 0xffff0000u); }
; DI u32x2 pack4(f32x4 v) { bf16x4_t r = __builtin_convertvector(v, bf16x4_t); return __builtin_bit_cast(u32x2, r); }
; DI int lane_id() { int l; asm volatile("v_mbcnt_lo_u32_b32 %0, -1, 0\n\tv_mbcnt_hi_u32_b32 %0, -1, %0" : "=v"(l)); return l; }
; DI void lru_local_unit(const Ctx& c, int u) {
;     ...
;         for (int it = 0; it < 8; ++it) { const int item = tid + it * NTHR, i = item >> 5, jc = item & 31;
;             *LP(u32x2, Waimg + trrow(i) * TS + jc * 8) = pack4(*(const f32x4*)(wa + i * 128 + jc * 4));
;             *LP(u32x2, Wximg + trrow(i) * TS + jc * 8) = pack4(*(const f32x4*)(wx + i * 128 + jc * 4)); }
;     }
;     {
;         const int tid = c.wid * 64 + lane_id(); const int tr = tid >> 4, cc = tid & 15, ch = cb + cc * 8;
;         float xin[7][8];
; #pragma unroll
;         for (int rr = 0; rr < 7; ++rr) { const int tl = 4 * tr - 3 + rr;
;             if (n == 0 && tl < 0) {
; #pragma unroll
;                 for (int k = 0; k < 8; ++k) xin[rr][k] = 0.f;
;             } else { const u32x4 v = *(const u32x4*)(proj + (size_t)(t0 + tl) * INC + 4 * RW + ch);
;                 xin[rr][0] = bflo(v.x); xin[rr][1] = bfhi(v.x); xin[rr][2] = bflo(v.y); xin[rr][3] = bfhi(v.y); xin[rr][4] = bflo(v.z); xin[rr][5] = bfhi(v.z); xin[rr][6] = bflo(v.w); xin[rr][7] = bfhi(v.w); } }
	v_cvt_pk_bf16_f32 v5, v14, v15
	v_cvt_pk_bf16_f32 v4, v12, v13
	v_add_u32_e32 v6, v6, v74
	ds_write_b64 v6, v[4:5]
	v_lshrrev_b32_e32 v6, 1, v68
	v_bitop3_b32 v6, v6, v68, 4 bitop3:0x6c
	v_mul_lo_u32 v6, v6, s50
	s_waitcnt vmcnt(11)
	v_cvt_pk_bf16_f32 v5, v18, v19
	v_cvt_pk_bf16_f32 v4, v16, v17
	v_add_u32_e32 v7, v6, v73
	ds_write_b64 v7, v[4:5]
	s_waitcnt vmcnt(10)
	v_cvt_pk_bf16_f32 v5, v22, v23
	v_cvt_pk_bf16_f32 v4, v20, v21
	v_add_u32_e32 v6, v6, v74
	ds_write_b64 v6, v[4:5]
	v_lshrrev_b32_e32 v6, 1, v69
	v_bitop3_b32 v6, v6, v69, 4 bitop3:0x6c
	v_mul_lo_u32 v6, v6, s50
	s_waitcnt vmcnt(9)
	v_cvt_pk_bf16_f32 v5, v26, v27
	v_cvt_pk_bf16_f32 v4, v24, v25
	v_add_u32_e32 v7, v6, v73
	ds_write_b64 v7, v[4:5]
	s_waitcnt vmcnt(8)
	v_cvt_pk_bf16_f32 v5, v30, v31
	v_cvt_pk_bf16_f32 v4, v28, v29
	v_add_u32_e32 v6, v6, v74
	ds_write_b64 v6, v[4:5]
	v_lshrrev_b32_e32 v6, 1, v70
	v_bitop3_b32 v6, v6, v70, 4 bitop3:0x6c
	v_mul_lo_u32 v6, v6, s50
	s_waitcnt vmcnt(7)
	v_cvt_pk_bf16_f32 v5, v34, v35
	v_cvt_pk_bf16_f32 v4, v32, v33
	v_add_u32_e32 v7, v6, v73
	ds_write_b64 v7, v[4:5]
	s_waitcnt vmcnt(6)
	v_cvt_pk_bf16_f32 v5, v38, v39
	v_cvt_pk_bf16_f32 v4, v36, v37
	v_add_u32_e32 v6, v6, v74
	ds_write_b64 v6, v[4:5]
	v_lshrrev_b32_e32 v6, 1, v71
	v_bitop3_b32 v6, v6, v71, 4 bitop3:0x6c
	v_mul_lo_u32 v6, v6, s50
	s_waitcnt vmcnt(5)
	v_cvt_pk_bf16_f32 v5, v42, v43
	v_cvt_pk_bf16_f32 v4, v40, v41
	v_add_u32_e32 v7, v6, v73
	ds_write_b64 v7, v[4:5]
	s_waitcnt vmcnt(4)
	v_cvt_pk_bf16_f32 v5, v46, v47
	v_cvt_pk_bf16_f32 v4, v44, v45
	v_add_u32_e32 v6, v6, v74
	ds_write_b64 v6, v[4:5]
	v_lshrrev_b32_e32 v6, 1, v72
	v_bitop3_b32 v6, v6, v72, 4 bitop3:0x6c
	v_mul_lo_u32 v6, v6, s50
	s_waitcnt vmcnt(3)
	v_cvt_pk_bf16_f32 v5, v50, v51
	v_cvt_pk_bf16_f32 v4, v48, v49
	v_add_u32_e32 v7, v6, v73
	ds_write_b64 v7, v[4:5]
	s_waitcnt vmcnt(2)
	v_cvt_pk_bf16_f32 v5, v54, v55
	v_cvt_pk_bf16_f32 v4, v52, v53
	v_add_u32_e32 v6, v6, v74
	ds_write_b64 v6, v[4:5]
	v_lshrrev_b32_e32 v6, 1, v75
	v_bitop3_b32 v6, v6, v75, 4 bitop3:0x6c
	v_mul_lo_u32 v6, v6, s50
	s_waitcnt vmcnt(1)
	v_cvt_pk_bf16_f32 v5, v58, v59
	v_cvt_pk_bf16_f32 v4, v56, v57
	v_add_u32_e32 v7, v6, v73
	ds_write_b64 v7, v[4:5]
	s_waitcnt vmcnt(0)
	v_cvt_pk_bf16_f32 v3, v2, v3
	v_cvt_pk_bf16_f32 v2, v0, v1
	v_add_u32_e32 v0, v6, v74
	ds_write_b64 v0, v[2:3]
	v_mbcnt_lo_u32_b32 v0, -1, 0
	v_mbcnt_hi_u32_b32 v0, -1, v0
	v_mov_b32_e32 v2, 0
	v_add_u32_e32 v1, s58, v0
	v_and_b32_e32 v57, 15, v0
	v_ashrrev_i32_e32 v41, 2, v1
	v_lshl_or_b32 v58, v57, 3, s70
	v_cmp_lt_i32_e32 vcc, 3, v41
	v_and_b32_e32 v56, -4, v41
	s_or_b64 s[28:29], s[28:29], vcc
	v_lshlrev_b32_e32 v88, 1, v58
	v_mov_b32_e32 v0, 0
	v_mov_b32_e32 v1, 0
	v_mov_b32_e32 v3, 0
	v_mov_b32_e32 v4, 0
	v_mov_b32_e32 v5, 0
	v_mov_b32_e32 v6, 0
	v_mov_b32_e32 v7, 0
	s_and_saveexec_b64 s[30:31], s[28:29]
	s_cbranch_execz .LBB0_135
	v_lshlrev_b32_e32 v6, 16, v168
	v_and_b32_e32 v7, 0xffff0000, v168
	v_lshlrev_b32_e32 v4, 16, v169
	v_and_b32_e32 v5, 0xffff0000, v169
	v_lshlrev_b32_e32 v2, 16, v170
	v_and_b32_e32 v3, 0xffff0000, v170
	v_lshlrev_b32_e32 v0, 16, v171
	v_and_b32_e32 v1, 0xffff0000, v171
.LBB0_135:
	s_or_b64 exec, exec, s[30:31]
	v_mov_b32_e32 v8, 0
	v_mov_b32_e32 v10, 0
	v_mov_b32_e32 v11, 0
	v_mov_b32_e32 v12, 0
	v_mov_b32_e32 v13, 0
	v_mov_b32_e32 v14, 0
	v_mov_b32_e32 v15, 0
	v_mov_b32_e32 v16, 0
	v_mov_b32_e32 v17, 0
	s_and_saveexec_b64 s[30:31], s[28:29]
	s_cbranch_execz .LBB0_137
	v_lshlrev_b32_e32 v16, 16, v172
	v_and_b32_e32 v17, 0xffff0000, v172
	v_lshlrev_b32_e32 v14, 16, v173
	v_and_b32_e32 v15, 0xffff0000, v173
	v_lshlrev_b32_e32 v12, 16, v174
	v_and_b32_e32 v13, 0xffff0000, v174
	v_lshlrev_b32_e32 v10, 16, v175
	v_and_b32_e32 v11, 0xffff0000, v175
.LBB0_137:
	s_or_b64 exec, exec, s[30:31]
	v_mov_b32_e32 v9, 0
	v_mov_b32_e32 v18, 0
	v_mov_b32_e32 v19, 0
	v_mov_b32_e32 v20, 0
	v_mov_b32_e32 v21, 0
	v_mov_b32_e32 v22, 0
	v_mov_b32_e32 v23, 0
	s_and_saveexec_b64 s[30:31], s[28:29]
	s_cbranch_execz .LBB0_139
	v_lshlrev_b32_e32 v22, 16, v176
	v_and_b32_e32 v23, 0xffff0000, v176
	v_lshlrev_b32_e32 v20, 16, v177
	v_and_b32_e32 v21, 0xffff0000, v177
	v_lshlrev_b32_e32 v18, 16, v178
	v_and_b32_e32 v19, 0xffff0000, v178
	v_lshlrev_b32_e32 v8, 16, v179
	v_and_b32_e32 v9, 0xffff0000, v179
.LBB0_139:
	s_or_b64 exec, exec, s[30:31]
	v_cmp_lt_i32_e32 vcc, -1, v41
	s_xor_b64 s[26:27], s[26:27], -1
	s_or_b64 s[26:27], s[26:27], vcc
	v_mov_b32_e32 v24, 0
	v_mov_b32_e32 v26, 0
	v_mov_b32_e32 v27, 0
	v_mov_b32_e32 v28, 0
	v_mov_b32_e32 v29, 0
	v_mov_b32_e32 v30, 0
	v_mov_b32_e32 v31, 0
	v_mov_b32_e32 v32, 0
	v_mov_b32_e32 v33, 0
	s_and_saveexec_b64 s[28:29], s[26:27]
	s_cbranch_execz .LBB0_141
	v_lshlrev_b32_e32 v32, 16, v180
	v_and_b32_e32 v33, 0xffff0000, v180
	v_lshlrev_b32_e32 v30, 16, v181
	v_and_b32_e32 v31, 0xffff0000, v181
	v_lshlrev_b32_e32 v28, 16, v182
	v_and_b32_e32 v29, 0xffff0000, v182
	v_lshlrev_b32_e32 v26, 16, v183
	v_and_b32_e32 v27, 0xffff0000, v183
.LBB0_141:
	s_or_b64 exec, exec, s[28:29]
	v_mov_b32_e32 v25, 0
	v_mov_b32_e32 v34, 0
	v_mov_b32_e32 v35, 0
	v_mov_b32_e32 v36, 0
	v_mov_b32_e32 v37, 0
	v_mov_b32_e32 v38, 0
	v_mov_b32_e32 v39, 0
	s_and_saveexec_b64 s[28:29], s[26:27]
	s_cbranch_execz .LBB0_143
	v_lshlrev_b32_e32 v38, 16, v184
	v_and_b32_e32 v39, 0xffff0000, v184
	v_lshlrev_b32_e32 v36, 16, v185
	v_and_b32_e32 v37, 0xffff0000, v185
	v_lshlrev_b32_e32 v34, 16, v186
	v_and_b32_e32 v35, 0xffff0000, v186
	v_lshlrev_b32_e32 v24, 16, v187
	v_and_b32_e32 v25, 0xffff0000, v187
.LBB0_143:
	s_or_b64 exec, exec, s[28:29]
	v_mov_b32_e32 v40, 0
	v_mov_b32_e32 v42, 0
	v_mov_b32_e32 v43, 0
	v_mov_b32_e32 v44, 0
	v_mov_b32_e32 v45, 0
	v_mov_b32_e32 v46, 0
	v_mov_b32_e32 v47, 0
	v_mov_b32_e32 v48, 0
	v_mov_b32_e32 v49, 0
	s_and_saveexec_b64 s[28:29], s[26:27]
	s_cbranch_execz .LBB0_145
	v_lshlrev_b32_e32 v48, 16, v188
	v_and_b32_e32 v49, 0xffff0000, v188
	v_lshlrev_b32_e32 v46, 16, v189
	v_and_b32_e32 v47, 0xffff0000, v189
	v_lshlrev_b32_e32 v44, 16, v190
	v_and_b32_e32 v45, 0xffff0000, v190
	v_lshlrev_b32_e32 v42, 16, v191
	v_and_b32_e32 v43, 0xffff0000, v191
.LBB0_145:
	s_or_b64 exec, exec, s[28:29]
	v_or_b32_e32 v59, 3, v41
	v_mov_b32_e32 v41, 0
	v_mov_b32_e32 v50, 0
	v_mov_b32_e32 v51, 0
	v_mov_b32_e32 v52, 0
	v_mov_b32_e32 v53, 0
	v_mov_b32_e32 v54, 0
	v_mov_b32_e32 v55, 0
	s_and_saveexec_b64 s[28:29], s[26:27]
	s_cbranch_execz .LBB0_147
	v_lshlrev_b32_e32 v54, 16, v192
	v_and_b32_e32 v55, 0xffff0000, v192
	v_lshlrev_b32_e32 v52, 16, v193
	v_and_b32_e32 v53, 0xffff0000, v193
	v_lshlrev_b32_e32 v50, 16, v194
	v_and_b32_e32 v51, 0xffff0000, v194
	v_lshlrev_b32_e32 v40, 16, v195
	v_and_b32_e32 v41, 0xffff0000, v195
